# index score phase: the next key tile's 8 fragment loads are issued (into v176-v207) right after the current tile's conversion, so the per-tile round trip overlaps the tile's MFMA work - stacked on v30
# baseline (speedup 1.0000x reference)
.LBB0_405:
	s_andn2_b64 vcc, exec, s[0:1]
	s_cbranch_vccnz .LBB0_449
	s_mov_b32 s100, 0
	s_mov_b32 s101, 0
	s_add_i32 s4, s80, 0xffffff70
	s_lshr_b32 s5, s4, 2
	v_mov_b32_e32 v45, v0
	s_and_b32 s6, s80, 3
	s_xor_b32 s12, s5, 63
	s_lshl_b32 s0, s6, 12
	s_lshl_b32 s1, s12, 6
	v_lshlrev_b32_e32 v1, 4, v45
	s_add_i32 s7, s1, s0
	v_and_b32_e32 v36, 0x3f0, v1
	v_ashrrev_i32_e32 v1, 6, v45
	v_add_u32_e32 v2, s7, v1
	v_readlane_b32 s8, v239, 24
	v_mul_lo_u32 v2, v2, s90
	v_readlane_b32 s9, v239, 25
	v_mov_b32_e32 v37, v3
	s_mov_b32 s1, 0x12a03000
	v_lshl_add_u64 v[4:5], v[2:3], 1, s[8:9]
	v_add_u32_e32 v2, 0x200, v45
	v_ashrrev_i32_e32 v38, 6, v2
	v_add_u32_e32 v2, s7, v38
	v_mul_lo_u32 v2, v2, s90
	v_lshl_add_u64 v[6:7], v[2:3], 1, s[8:9]
	v_add_u32_e32 v2, 0x400, v45
	v_ashrrev_i32_e32 v39, 6, v2
	v_add_u32_e32 v2, s7, v39
	v_mul_lo_u32 v2, v2, s90
	v_lshl_add_u64 v[12:13], v[2:3], 1, s[8:9]
	v_add_u32_e32 v2, 0x600, v45
	v_ashrrev_i32_e32 v40, 6, v2
	v_add_u32_e32 v2, s7, v40
	v_mul_lo_u32 v2, v2, s90
	v_lshl_add_u64 v[14:15], v[2:3], 1, s[8:9]
	v_add_u32_e32 v2, 0x800, v45
	v_ashrrev_i32_e32 v41, 6, v2
	v_lshl_add_u64 v[4:5], v[4:5], 0, v[36:37]
	v_add_u32_e32 v2, s7, v41
	v_add_co_u32_e32 v4, vcc, s1, v4
	v_mul_lo_u32 v2, v2, s90
	s_nop 0
	v_addc_co_u32_e32 v5, vcc, 0, v5, vcc
	v_lshl_add_u64 v[6:7], v[6:7], 0, v[36:37]
	v_lshl_add_u64 v[20:21], v[2:3], 1, s[8:9]
	v_add_u32_e32 v2, 0xa00, v45
	v_add_co_u32_e32 v8, vcc, s1, v6
	v_ashrrev_i32_e32 v42, 6, v2
	s_nop 0
	v_addc_co_u32_e32 v9, vcc, 0, v7, vcc
	v_lshl_add_u64 v[12:13], v[12:13], 0, v[36:37]
	v_add_u32_e32 v2, s7, v42
	v_add_co_u32_e32 v12, vcc, s1, v12
	v_mul_lo_u32 v2, v2, s90
	s_nop 0
	v_addc_co_u32_e32 v13, vcc, 0, v13, vcc
	v_lshl_add_u64 v[14:15], v[14:15], 0, v[36:37]
	v_lshl_add_u64 v[22:23], v[2:3], 1, s[8:9]
	v_add_u32_e32 v2, 0xc00, v45
	v_add_co_u32_e32 v16, vcc, s1, v14
	v_ashrrev_i32_e32 v43, 6, v2
	s_nop 0
	v_addc_co_u32_e32 v17, vcc, 0, v15, vcc
	v_lshl_add_u64 v[20:21], v[20:21], 0, v[36:37]
	v_add_u32_e32 v2, s7, v43
	v_add_co_u32_e32 v20, vcc, s1, v20
	v_mul_lo_u32 v2, v2, s90
	global_load_dwordx4 v[4:7], v[4:5], off
	s_nop 0
	global_load_dwordx4 v[8:11], v[8:9], off
	v_addc_co_u32_e32 v21, vcc, 0, v21, vcc
	v_lshl_add_u64 v[22:23], v[22:23], 0, v[36:37]
	v_lshl_add_u64 v[28:29], v[2:3], 1, s[8:9]
	v_add_u32_e32 v2, 0xe00, v45
	v_add_co_u32_e32 v24, vcc, s1, v22
	v_ashrrev_i32_e32 v46, 6, v2
	global_load_dwordx4 v[12:15], v[12:13], off
	s_nop 0
	global_load_dwordx4 v[16:19], v[16:17], off
	v_addc_co_u32_e32 v25, vcc, 0, v23, vcc
	v_lshl_add_u64 v[28:29], v[28:29], 0, v[36:37]
	v_add_u32_e32 v2, s7, v46
	v_add_co_u32_e32 v28, vcc, s1, v28
	v_mul_lo_u32 v2, v2, s90
	global_load_dwordx4 v[20:23], v[20:21], off
	s_nop 0
	global_load_dwordx4 v[24:27], v[24:25], off
	v_addc_co_u32_e32 v29, vcc, 0, v29, vcc
	v_lshl_add_u64 v[32:33], v[2:3], 1, s[8:9]
	global_load_dwordx4 v[28:31], v[28:29], off
	v_lshl_add_u64 v[32:33], v[32:33], 0, v[36:37]
	v_add_co_u32_e32 v32, vcc, 0x12a03000, v32
	v_readlane_b32 s10, v239, 26
	s_nop 0
	v_addc_co_u32_e32 v33, vcc, 0, v33, vcc
	global_load_dwordx4 v[32:35], v[32:33], off
	v_readfirstlane_b32 s1, v45
	s_sub_i32 s51, 64, s5
	s_mov_b32 s10, s7
	s_ashr_i32 s36, s1, 6
	s_lshl_b32 s37, s51, 6
	v_writelane_b32 v236, s6, 43
	s_mul_i32 s1, s6, 0x2080000
	v_readlane_b32 s6, v237, 26
	v_readlane_b32 s7, v237, 27
	s_add_u32 s1, s6, s1
	s_addc_u32 s6, s7, 0
	s_mul_i32 s7, s51, s12
	s_lshl_b32 s7, s7, 13
	s_and_b32 s7, s7, 0x3ffc000
	s_add_u32 s8, s1, s7
	v_add_u32_e32 v2, 0, v36
	s_addc_u32 s9, s6, 0
	v_mad_u64_u32 v[36:37], s[6:7], v1, s91, v[2:3]
	v_writelane_b32 v236, s12, 44
	v_and_b32_e32 v44, 63, v45
	v_writelane_b32 v236, s8, 45
	v_readlane_b32 s11, v239, 27
	s_waitcnt vmcnt(7)
	ds_write_b128 v36, v[4:7]
	v_mad_u64_u32 v[4:5], s[6:7], v38, s91, v[2:3]
	s_waitcnt vmcnt(6)
	ds_write_b128 v4, v[8:11]
	v_mad_u64_u32 v[4:5], s[6:7], v39, s91, v[2:3]
	v_writelane_b32 v236, s9, 46
	s_waitcnt vmcnt(5)
	ds_write_b128 v4, v[12:15]
	v_mad_u64_u32 v[4:5], s[6:7], v40, s91, v[2:3]
	s_waitcnt vmcnt(4)
	ds_write_b128 v4, v[16:19]
	v_mad_u64_u32 v[4:5], s[6:7], v41, s91, v[2:3]
	s_waitcnt vmcnt(3)
	ds_write_b128 v4, v[20:23]
	v_mad_u64_u32 v[4:5], s[6:7], v42, s91, v[2:3]
	s_waitcnt vmcnt(2)
	ds_write_b128 v4, v[24:27]
	v_mad_u64_u32 v[4:5], s[6:7], v43, s91, v[2:3]
	s_waitcnt vmcnt(1)
	ds_write_b128 v4, v[28:31]
	v_mad_u64_u32 v[4:5], s[6:7], v46, s91, v[2:3]
	s_lshl_b32 s6, s51, 1
	s_cmp_ge_i32 s36, s6
	s_waitcnt vmcnt(0)
	ds_write_b128 v4, v[32:35]
	s_waitcnt lgkmcnt(0)
	s_barrier
	s_cbranch_scc1 .LBB0_411
	v_and_b32_e32 v1, 31, v45
	v_or_b32_e32 v101, s0, v1
	v_lshrrev_b32_e32 v2, 1, v44
	v_readlane_b32 s0, v236, 45
	v_and_b32_e32 v2, 16, v2
	v_readlane_b32 s1, v236, 46
	v_add_u32_e32 v135, 0, v2
	v_or_b32_e32 v168, s10, v1
	v_lshl_add_u64 v[46:47], s[0:1], 0, v[2:3]
	v_and_b32_e32 v2, 32, v44
	v_lshl_add_u64 v[48:49], s[2:3], 0, v[2:3]
	s_mov_b32 s7, s36
.LBB0_408:
	s_lshl_b32 s0, s7, 5
	s_cmp_eq_u32 s101, 1
	s_cbranch_scc1 .Lkh_have
	v_add_lshl_u32 v2, v101, s0, 9
	v_lshl_add_u64 v[12:13], v[2:3], 2, v[48:49]
	global_load_dwordx4 v[176:179], v[12:13], off offset:80
	global_load_dwordx4 v[180:183], v[12:13], off offset:64
	global_load_dwordx4 v[184:187], v[12:13], off offset:144
	global_load_dwordx4 v[188:191], v[12:13], off offset:128
	global_load_dwordx4 v[192:195], v[12:13], off offset:208
	global_load_dwordx4 v[196:199], v[12:13], off offset:192
	global_load_dwordx4 v[200:203], v[12:13], off offset:272
	global_load_dwordx4 v[204:207], v[12:13], off offset:256
	s_waitcnt vmcnt(0)
	s_branch .Lkh_cvt

.Lkh_cvt:
	v_cvt_pk_bf16_f32 v22, v176, v177
	v_cvt_pk_bf16_f32 v23, v178, v179
	v_cvt_pk_bf16_f32 v20, v180, v181
	v_cvt_pk_bf16_f32 v21, v182, v183
	v_cvt_pk_bf16_f32 v26, v184, v185
	v_cvt_pk_bf16_f32 v27, v186, v187
	v_cvt_pk_bf16_f32 v24, v188, v189
	v_cvt_pk_bf16_f32 v25, v190, v191
	v_cvt_pk_bf16_f32 v30, v192, v193
	v_cvt_pk_bf16_f32 v31, v194, v195
	v_cvt_pk_bf16_f32 v28, v196, v197
	v_cvt_pk_bf16_f32 v29, v198, v199
	v_cvt_pk_bf16_f32 v34, v200, v201
	v_cvt_pk_bf16_f32 v35, v202, v203
	v_cvt_pk_bf16_f32 v32, v204, v205
	v_cvt_pk_bf16_f32 v33, v206, v207
	s_mov_b32 s101, 0
	s_add_i32 s1, s7, 8
	s_cmp_lt_i32 s1, s6
	s_cbranch_scc0 .Lkh_nopf
	s_lshl_b32 s1, s1, 5
	v_add_lshl_u32 v2, v101, s1, 9
	v_lshl_add_u64 v[12:13], v[2:3], 2, v[48:49]
	global_load_dwordx4 v[176:179], v[12:13], off offset:80
	global_load_dwordx4 v[180:183], v[12:13], off offset:64
	global_load_dwordx4 v[184:187], v[12:13], off offset:144
	global_load_dwordx4 v[188:191], v[12:13], off offset:128
	global_load_dwordx4 v[192:195], v[12:13], off offset:208
	global_load_dwordx4 v[196:199], v[12:13], off offset:192
	global_load_dwordx4 v[200:203], v[12:13], off offset:272
	global_load_dwordx4 v[204:207], v[12:13], off offset:256
	s_mov_b32 s101, 1
.Lkh_nopf:
	s_ashr_i32 s1, s0, 31
	v_lshl_add_u64 v[50:51], s[0:1], 2, v[46:47]
	s_mov_b32 s8, 0
	s_mov_b64 s[0:1], -1
